# P5 pool-GEMM epilogue: gain pieces loaded and scaled once, 16 per-round reloads and vmcnt(0) waits removed
# baseline (speedup 1.0000x reference)
;     __device__ __forceinline__ void operator()(const f32x4 (&acc)[2][2][4][2], const PoolU& u, int wr, int wc, int fr, int fq) const {
;     ...
;             for (int m = 0; m < 4; ++m) { unsigned char* rp = ymix + (size_t)(row0 + ai * 128 + m * 16) * 2048 + 1024 + c0;
; #pragma unroll
;                 for (int bj = 0; bj < 2; ++bj) { const f32x4 s0 = *(const f32x4*)(scale + c0 + bj * 128) * SC_Y, s1 = *(const f32x4*)(scale + c0 + bj * 128 + 4) * SC_Y;
;                     const f32x4 v0 = acc[ai][bj][m][0] * s0, v1 = acc[ai][bj][m][1] * s1;
;                     v2u o; o.x = pk4_fp8(v0[0], v0[1], v0[2], v0[3]); o.y = pk4_fp8(v1[0], v1[1], v1[2], v1[3]);
;                     *(v2u*)(rp + bj * 128) = o; } }
.LBB0_949:
	v_mov_b32_e32 v150, v0
	v_mov_b32_e32 v164, 0
	v_lshrrev_b32_e32 v146, 1, v150
	v_and_b32_e32 v146, 0x78, v146
	v_lshl_or_b32 v148, s59, 8, v146
	v_ashrrev_i32_e32 v149, 31, v148
	v_lshl_add_u64 v[146:147], v[148:149], 2, s[54:55]
	global_load_dwordx4 v[172:175], v[146:147], off
	global_load_dwordx4 v[180:183], v[146:147], off offset:16
	global_load_dwordx4 v[188:191], v[146:147], off offset:512
	global_load_dwordx4 v[196:199], v[146:147], off offset:528
	v_mov_b32_e32 v165, 0
	v_ashrrev_i32_e32 v151, 2, v150
	v_and_b32_e32 v151, 0xffffffc0, v151
	v_lshl_add_u32 v151, s30, 8, v151
	v_and_or_b32 v150, v150, 15, v151
	v_ashrrev_i32_e32 v151, 31, v150
	s_mov_b64 s[2:3], 0x40000
	s_andn2_b64 vcc, exec, s[28:29]
	s_waitcnt vmcnt(0)
	v_pk_mul_f32 v[172:173], v[172:173], s[14:15] op_sel_hi:[1,0]
	v_pk_mul_f32 v[174:175], v[174:175], s[14:15] op_sel_hi:[1,0]
	v_pk_mul_f32 v[180:181], v[180:181], s[14:15] op_sel_hi:[1,0]
	v_pk_mul_f32 v[182:183], v[182:183], s[14:15] op_sel_hi:[1,0]
	v_pk_mul_f32 v[188:189], v[188:189], s[14:15] op_sel_hi:[1,0]
	v_pk_mul_f32 v[190:191], v[190:191], s[14:15] op_sel_hi:[1,0]
	v_pk_mul_f32 v[196:197], v[196:197], s[14:15] op_sel_hi:[1,0]
	v_pk_mul_f32 v[198:199], v[198:199], s[14:15] op_sel_hi:[1,0]
	v_pk_mul_f32 v[126:127], v[126:127], v[172:173]
	v_pk_mul_f32 v[122:123], v[122:123], v[180:181]
	v_med3_f32 v126, v126, s51, v155
	v_med3_f32 v127, v127, s51, v155
	v_med3_f32 v122, v122, s51, v155
	v_med3_f32 v123, v123, s51, v155
	v_cvt_pk_fp8_f32 v164, v126, v127
	v_cvt_pk_fp8_f32 v165, v122, v123
	v_pk_mul_f32 v[128:129], v[128:129], v[174:175]
	v_pk_mul_f32 v[124:125], v[124:125], v[182:183]
	v_med3_f32 v128, v128, s51, v155
	v_med3_f32 v129, v129, s51, v155
	v_med3_f32 v122, v124, s51, v155
	v_med3_f32 v123, v125, s51, v155
	v_cvt_pk_fp8_f32 v164, v128, v129 op_sel:[0,0,1]
	v_cvt_pk_fp8_f32 v165, v122, v123 op_sel:[0,0,1]
	v_lshlrev_b64 v[122:123], 11, v[150:151]
	v_lshl_add_u64 v[122:123], s[8:9], 0, v[122:123]
	v_lshl_add_u64 v[122:123], v[122:123], 0, v[148:149]
	global_store_dwordx2 v[122:123], v[164:165], off offset:1024
	v_mov_b32_e32 v128, 0
	v_mov_b32_e32 v129, 0
	v_pk_mul_f32 v[118:119], v[118:119], v[188:189]
	v_pk_mul_f32 v[114:115], v[114:115], v[196:197]
	v_med3_f32 v118, v118, s51, v155
	v_med3_f32 v119, v119, s51, v155
	v_med3_f32 v114, v114, s51, v155
	v_med3_f32 v115, v115, s51, v155
	v_cvt_pk_fp8_f32 v128, v118, v119
	v_cvt_pk_fp8_f32 v129, v114, v115
	v_pk_mul_f32 v[120:121], v[120:121], v[190:191]
	v_pk_mul_f32 v[116:117], v[116:117], v[198:199]
	v_med3_f32 v120, v120, s51, v155
	v_med3_f32 v121, v121, s51, v155
	v_med3_f32 v114, v116, s51, v155
	v_med3_f32 v115, v117, s51, v155
	v_cvt_pk_fp8_f32 v128, v120, v121 op_sel:[0,0,1]
	v_cvt_pk_fp8_f32 v129, v114, v115 op_sel:[0,0,1]
	v_mov_b32_e32 v124, 0
	v_mov_b32_e32 v125, 0
	v_or_b32_e32 v126, 16, v150
	global_store_dwordx2 v[122:123], v[128:129], off offset:1152
	v_ashrrev_i32_e32 v127, 31, v126
	v_pk_mul_f32 v[110:111], v[110:111], v[172:173]
	v_pk_mul_f32 v[106:107], v[106:107], v[180:181]
	v_med3_f32 v110, v110, s51, v155
	v_med3_f32 v111, v111, s51, v155
	v_med3_f32 v106, v106, s51, v155
	v_med3_f32 v107, v107, s51, v155
	v_cvt_pk_fp8_f32 v124, v110, v111
	v_cvt_pk_fp8_f32 v125, v106, v107
	v_pk_mul_f32 v[112:113], v[112:113], v[174:175]
	v_pk_mul_f32 v[108:109], v[108:109], v[182:183]
	v_med3_f32 v112, v112, s51, v155
	v_med3_f32 v113, v113, s51, v155
	v_med3_f32 v106, v108, s51, v155
	v_med3_f32 v107, v109, s51, v155
	v_cvt_pk_fp8_f32 v124, v112, v113 op_sel:[0,0,1]
	v_cvt_pk_fp8_f32 v125, v106, v107 op_sel:[0,0,1]
	v_lshlrev_b64 v[106:107], 11, v[126:127]
	v_lshl_add_u64 v[106:107], s[8:9], 0, v[106:107]
	v_lshl_add_u64 v[114:115], v[106:107], 0, v[148:149]
	global_store_dwordx2 v[114:115], v[124:125], off offset:1024
	v_mov_b32_e32 v116, 0
	v_mov_b32_e32 v117, 0
	v_pk_mul_f32 v[102:103], v[102:103], v[188:189]
	v_pk_mul_f32 v[98:99], v[98:99], v[196:197]
	v_med3_f32 v102, v102, s51, v155
	v_med3_f32 v103, v103, s51, v155
	v_med3_f32 v98, v98, s51, v155
	v_med3_f32 v99, v99, s51, v155
	v_cvt_pk_fp8_f32 v116, v102, v103
	v_cvt_pk_fp8_f32 v117, v98, v99
	v_pk_mul_f32 v[104:105], v[104:105], v[190:191]
	v_pk_mul_f32 v[100:101], v[100:101], v[198:199]
	v_med3_f32 v104, v104, s51, v155
	v_med3_f32 v105, v105, s51, v155
	v_med3_f32 v98, v100, s51, v155
	v_med3_f32 v99, v101, s51, v155
	v_cvt_pk_fp8_f32 v116, v104, v105 op_sel:[0,0,1]
	v_cvt_pk_fp8_f32 v117, v98, v99 op_sel:[0,0,1]
	v_mov_b32_e32 v106, 0
	v_mov_b32_e32 v107, 0
	v_or_b32_e32 v108, 32, v150
	global_store_dwordx2 v[114:115], v[116:117], off offset:1152
	v_ashrrev_i32_e32 v109, 31, v108
	v_pk_mul_f32 v[94:95], v[94:95], v[172:173]
	v_pk_mul_f32 v[90:91], v[90:91], v[180:181]
	v_med3_f32 v94, v94, s51, v155
	v_med3_f32 v95, v95, s51, v155
	v_med3_f32 v90, v90, s51, v155
	v_med3_f32 v91, v91, s51, v155
	v_cvt_pk_fp8_f32 v106, v94, v95
	v_cvt_pk_fp8_f32 v107, v90, v91
	v_pk_mul_f32 v[96:97], v[96:97], v[174:175]
	v_pk_mul_f32 v[92:93], v[92:93], v[182:183]
	v_med3_f32 v96, v96, s51, v155
	v_med3_f32 v97, v97, s51, v155
	v_med3_f32 v90, v92, s51, v155
	v_med3_f32 v91, v93, s51, v155
	v_cvt_pk_fp8_f32 v106, v96, v97 op_sel:[0,0,1]
	v_cvt_pk_fp8_f32 v107, v90, v91 op_sel:[0,0,1]
	v_lshlrev_b64 v[90:91], 11, v[108:109]
	v_lshl_add_u64 v[90:91], s[8:9], 0, v[90:91]
	v_lshl_add_u64 v[98:99], v[90:91], 0, v[148:149]
	global_store_dwordx2 v[98:99], v[106:107], off offset:1024
	v_mov_b32_e32 v100, 0
	v_mov_b32_e32 v101, 0
	v_pk_mul_f32 v[86:87], v[86:87], v[188:189]
	v_pk_mul_f32 v[82:83], v[82:83], v[196:197]
	v_med3_f32 v86, v86, s51, v155
	v_med3_f32 v87, v87, s51, v155
;     __device__ __forceinline__ void operator()(const f32x4 (&acc)[2][2][4][2], const PoolU& u, int wr, int wc, int fr, int fq) const {
;     ...
;             for (int m = 0; m < 4; ++m) { unsigned char* rp = ymix + (size_t)(row0 + ai * 128 + m * 16) * 2048 + 1024 + c0;
; #pragma unroll
;                 for (int bj = 0; bj < 2; ++bj) { const f32x4 s0 = *(const f32x4*)(scale + c0 + bj * 128) * SC_Y, s1 = *(const f32x4*)(scale + c0 + bj * 128 + 4) * SC_Y;
;                     const f32x4 v0 = acc[ai][bj][m][0] * s0, v1 = acc[ai][bj][m][1] * s1;
;                     v2u o; o.x = pk4_fp8(v0[0], v0[1], v0[2], v0[3]); o.y = pk4_fp8(v1[0], v1[1], v1[2], v1[3]);
;                     *(v2u*)(rp + bj * 128) = o; } }
	v_med3_f32 v82, v82, s51, v155
	v_med3_f32 v83, v83, s51, v155
	v_cvt_pk_fp8_f32 v100, v86, v87
	v_cvt_pk_fp8_f32 v101, v82, v83
	v_pk_mul_f32 v[88:89], v[88:89], v[190:191]
	v_pk_mul_f32 v[84:85], v[84:85], v[198:199]
	v_med3_f32 v88, v88, s51, v155
	v_med3_f32 v89, v89, s51, v155
	v_med3_f32 v82, v84, s51, v155
	v_med3_f32 v83, v85, s51, v155
	v_cvt_pk_fp8_f32 v100, v88, v89 op_sel:[0,0,1]
	v_cvt_pk_fp8_f32 v101, v82, v83 op_sel:[0,0,1]
	v_mov_b32_e32 v90, 0
	v_mov_b32_e32 v91, 0
	v_or_b32_e32 v92, 48, v150
	global_store_dwordx2 v[98:99], v[100:101], off offset:1152
	v_ashrrev_i32_e32 v93, 31, v92
	v_pk_mul_f32 v[78:79], v[78:79], v[172:173]
	v_pk_mul_f32 v[74:75], v[74:75], v[180:181]
	v_med3_f32 v78, v78, s51, v155
	v_med3_f32 v79, v79, s51, v155
	v_med3_f32 v74, v74, s51, v155
	v_med3_f32 v75, v75, s51, v155
	v_cvt_pk_fp8_f32 v90, v78, v79
	v_cvt_pk_fp8_f32 v91, v74, v75
	v_pk_mul_f32 v[80:81], v[80:81], v[174:175]
	v_pk_mul_f32 v[76:77], v[76:77], v[182:183]
	v_med3_f32 v80, v80, s51, v155
	v_med3_f32 v81, v81, s51, v155
	v_med3_f32 v74, v76, s51, v155
	v_med3_f32 v75, v77, s51, v155
	v_cvt_pk_fp8_f32 v90, v80, v81 op_sel:[0,0,1]
	v_cvt_pk_fp8_f32 v91, v74, v75 op_sel:[0,0,1]
	v_lshlrev_b64 v[74:75], 11, v[92:93]
	v_lshl_add_u64 v[74:75], s[8:9], 0, v[74:75]
	v_lshl_add_u64 v[82:83], v[74:75], 0, v[148:149]
	global_store_dwordx2 v[82:83], v[90:91], off offset:1024
	v_mov_b32_e32 v84, 0
	v_mov_b32_e32 v85, 0
	v_pk_mul_f32 v[70:71], v[70:71], v[188:189]
	v_pk_mul_f32 v[66:67], v[66:67], v[196:197]
	v_med3_f32 v70, v70, s51, v155
	v_med3_f32 v71, v71, s51, v155
	v_med3_f32 v66, v66, s51, v155
	v_med3_f32 v67, v67, s51, v155
	v_cvt_pk_fp8_f32 v84, v70, v71
	v_cvt_pk_fp8_f32 v85, v66, v67
	v_pk_mul_f32 v[72:73], v[72:73], v[190:191]
	v_pk_mul_f32 v[68:69], v[68:69], v[198:199]
	v_med3_f32 v72, v72, s51, v155
	v_med3_f32 v73, v73, s51, v155
	v_med3_f32 v66, v68, s51, v155
	v_med3_f32 v67, v69, s51, v155
	v_cvt_pk_fp8_f32 v84, v72, v73 op_sel:[0,0,1]
	v_cvt_pk_fp8_f32 v85, v66, v67 op_sel:[0,0,1]
	v_mov_b32_e32 v74, 0
	v_mov_b32_e32 v75, 0
	global_store_dwordx2 v[82:83], v[84:85], off offset:1152
	v_pk_mul_f32 v[62:63], v[62:63], v[172:173]
	v_pk_mul_f32 v[58:59], v[58:59], v[180:181]
	v_med3_f32 v62, v62, s51, v155
	v_med3_f32 v63, v63, s51, v155
	v_med3_f32 v58, v58, s51, v155
	v_med3_f32 v59, v59, s51, v155
	v_cvt_pk_fp8_f32 v74, v62, v63
	v_cvt_pk_fp8_f32 v75, v58, v59
	v_pk_mul_f32 v[64:65], v[64:65], v[174:175]
	v_pk_mul_f32 v[60:61], v[60:61], v[182:183]
	v_med3_f32 v64, v64, s51, v155
	v_med3_f32 v65, v65, s51, v155
	v_med3_f32 v58, v60, s51, v155
	v_med3_f32 v59, v61, s51, v155
	v_cvt_pk_fp8_f32 v74, v64, v65 op_sel:[0,0,1]
	v_cvt_pk_fp8_f32 v75, v58, v59 op_sel:[0,0,1]
	v_lshl_add_u64 v[66:67], v[122:123], 0, s[2:3]
	v_mov_b32_e32 v68, 0
	v_mov_b32_e32 v69, 0
	global_store_dwordx2 v[66:67], v[74:75], off offset:1024
	s_mov_b64 s[2:3], -1
	v_pk_mul_f32 v[54:55], v[54:55], v[188:189]
	v_pk_mul_f32 v[50:51], v[50:51], v[196:197]
	v_med3_f32 v54, v54, s51, v155
	v_med3_f32 v55, v55, s51, v155
	v_med3_f32 v50, v50, s51, v155
	v_med3_f32 v51, v51, s51, v155
	v_cvt_pk_fp8_f32 v68, v54, v55
	v_cvt_pk_fp8_f32 v69, v50, v51
	v_pk_mul_f32 v[56:57], v[56:57], v[190:191]
	v_pk_mul_f32 v[52:53], v[52:53], v[198:199]
	v_med3_f32 v56, v56, s51, v155
	v_med3_f32 v57, v57, s51, v155
	v_med3_f32 v50, v52, s51, v155
	v_med3_f32 v51, v53, s51, v155
	v_cvt_pk_fp8_f32 v68, v56, v57 op_sel:[0,0,1]
	v_cvt_pk_fp8_f32 v69, v50, v51 op_sel:[0,0,1]
	v_mov_b32_e32 v58, 0
	v_mov_b32_e32 v59, 0
	global_store_dwordx2 v[66:67], v[68:69], off offset:1152
	v_pk_mul_f32 v[46:47], v[46:47], v[172:173]
	v_pk_mul_f32 v[42:43], v[42:43], v[180:181]
	v_med3_f32 v46, v46, s51, v155
	v_med3_f32 v47, v47, s51, v155
	v_med3_f32 v42, v42, s51, v155
	v_med3_f32 v43, v43, s51, v155
	v_cvt_pk_fp8_f32 v58, v46, v47
	v_cvt_pk_fp8_f32 v59, v42, v43
	v_pk_mul_f32 v[48:49], v[48:49], v[174:175]
	v_pk_mul_f32 v[44:45], v[44:45], v[182:183]
;     __device__ __forceinline__ void operator()(const f32x4 (&acc)[2][2][4][2], const PoolU& u, int wr, int wc, int fr, int fq) const {
;     ...
;             for (int m = 0; m < 4; ++m) { unsigned char* rp = ymix + (size_t)(row0 + ai * 128 + m * 16) * 2048 + 1024 + c0;
; #pragma unroll
;                 for (int bj = 0; bj < 2; ++bj) { const f32x4 s0 = *(const f32x4*)(scale + c0 + bj * 128) * SC_Y, s1 = *(const f32x4*)(scale + c0 + bj * 128 + 4) * SC_Y;
;                     const f32x4 v0 = acc[ai][bj][m][0] * s0, v1 = acc[ai][bj][m][1] * s1;
;                     v2u o; o.x = pk4_fp8(v0[0], v0[1], v0[2], v0[3]); o.y = pk4_fp8(v1[0], v1[1], v1[2], v1[3]);
;                     *(v2u*)(rp + bj * 128) = o; } }
	v_med3_f32 v48, v48, s51, v155
	v_med3_f32 v49, v49, s51, v155
	v_med3_f32 v42, v44, s51, v155
	v_med3_f32 v43, v45, s51, v155
	v_cvt_pk_fp8_f32 v58, v48, v49 op_sel:[0,0,1]
	v_cvt_pk_fp8_f32 v59, v42, v43 op_sel:[0,0,1]
	v_lshl_add_u64 v[50:51], v[122:123], 0, s[16:17]
	v_mov_b32_e32 v52, 0
	v_mov_b32_e32 v53, 0
	global_store_dwordx2 v[50:51], v[58:59], off offset:1024
	v_pk_mul_f32 v[38:39], v[38:39], v[188:189]
	v_pk_mul_f32 v[34:35], v[34:35], v[196:197]
	v_med3_f32 v38, v38, s51, v155
	v_med3_f32 v39, v39, s51, v155
	v_med3_f32 v34, v34, s51, v155
	v_med3_f32 v35, v35, s51, v155
	v_cvt_pk_fp8_f32 v52, v38, v39
	v_cvt_pk_fp8_f32 v53, v34, v35
	v_pk_mul_f32 v[40:41], v[40:41], v[190:191]
	v_pk_mul_f32 v[36:37], v[36:37], v[198:199]
	v_med3_f32 v40, v40, s51, v155
	v_med3_f32 v41, v41, s51, v155
	v_med3_f32 v34, v36, s51, v155
	v_med3_f32 v35, v37, s51, v155
	v_cvt_pk_fp8_f32 v52, v40, v41 op_sel:[0,0,1]
	v_cvt_pk_fp8_f32 v53, v34, v35 op_sel:[0,0,1]
	v_mov_b32_e32 v42, 0
	v_mov_b32_e32 v43, 0
	global_store_dwordx2 v[50:51], v[52:53], off offset:1152
	v_pk_mul_f32 v[30:31], v[30:31], v[172:173]
	v_pk_mul_f32 v[26:27], v[26:27], v[180:181]
	v_med3_f32 v30, v30, s51, v155
	v_med3_f32 v31, v31, s51, v155
	v_med3_f32 v26, v26, s51, v155
	v_med3_f32 v27, v27, s51, v155
	v_cvt_pk_fp8_f32 v42, v30, v31
	v_cvt_pk_fp8_f32 v43, v26, v27
	v_pk_mul_f32 v[32:33], v[32:33], v[174:175]
	v_pk_mul_f32 v[28:29], v[28:29], v[182:183]
	v_med3_f32 v32, v32, s51, v155
	v_med3_f32 v33, v33, s51, v155
	v_med3_f32 v26, v28, s51, v155
	v_med3_f32 v27, v29, s51, v155
	v_cvt_pk_fp8_f32 v42, v32, v33 op_sel:[0,0,1]
	v_cvt_pk_fp8_f32 v43, v26, v27 op_sel:[0,0,1]
	v_lshl_add_u64 v[34:35], v[122:123], 0, s[18:19]
	v_mov_b32_e32 v36, 0
	v_mov_b32_e32 v37, 0
	global_store_dwordx2 v[34:35], v[42:43], off offset:1024
	v_pk_mul_f32 v[22:23], v[22:23], v[188:189]
	v_pk_mul_f32 v[18:19], v[18:19], v[196:197]
	v_med3_f32 v22, v22, s51, v155
	v_med3_f32 v23, v23, s51, v155
	v_med3_f32 v18, v18, s51, v155
	v_med3_f32 v19, v19, s51, v155
	v_cvt_pk_fp8_f32 v36, v22, v23
	v_cvt_pk_fp8_f32 v37, v18, v19
	v_pk_mul_f32 v[24:25], v[24:25], v[190:191]
	v_pk_mul_f32 v[20:21], v[20:21], v[198:199]
	v_med3_f32 v24, v24, s51, v155
	v_med3_f32 v25, v25, s51, v155
	v_med3_f32 v18, v20, s51, v155
	v_med3_f32 v19, v21, s51, v155
	v_cvt_pk_fp8_f32 v36, v24, v25 op_sel:[0,0,1]
	v_cvt_pk_fp8_f32 v37, v18, v19 op_sel:[0,0,1]
	v_mov_b32_e32 v26, 0
	v_mov_b32_e32 v27, 0
	global_store_dwordx2 v[34:35], v[36:37], off offset:1152
	v_pk_mul_f32 v[14:15], v[14:15], v[172:173]
	v_pk_mul_f32 v[10:11], v[10:11], v[180:181]
	v_med3_f32 v14, v14, s51, v155
	v_med3_f32 v15, v15, s51, v155
	v_med3_f32 v10, v10, s51, v155
	v_med3_f32 v11, v11, s51, v155
	v_cvt_pk_fp8_f32 v26, v14, v15
	v_cvt_pk_fp8_f32 v27, v10, v11
	v_pk_mul_f32 v[16:17], v[16:17], v[174:175]
	v_pk_mul_f32 v[12:13], v[12:13], v[182:183]
	v_med3_f32 v16, v16, s51, v155
	v_med3_f32 v17, v17, s51, v155
	v_med3_f32 v10, v12, s51, v155
	v_med3_f32 v11, v13, s51, v155
	v_cvt_pk_fp8_f32 v26, v16, v17 op_sel:[0,0,1]
	v_cvt_pk_fp8_f32 v27, v10, v11 op_sel:[0,0,1]
	v_lshl_add_u64 v[18:19], v[122:123], 0, s[20:21]
	v_mov_b32_e32 v20, 0
	v_mov_b32_e32 v21, 0
	global_store_dwordx2 v[18:19], v[26:27], off offset:1024
	v_pk_mul_f32 v[6:7], v[6:7], v[188:189]
	v_pk_mul_f32 v[2:3], v[2:3], v[196:197]
	v_med3_f32 v6, v6, s51, v155
	v_med3_f32 v7, v7, s51, v155
	v_med3_f32 v2, v2, s51, v155
	v_med3_f32 v3, v3, s51, v155
	v_cvt_pk_fp8_f32 v20, v6, v7
	v_cvt_pk_fp8_f32 v21, v2, v3
	v_pk_mul_f32 v[8:9], v[8:9], v[190:191]
	v_pk_mul_f32 v[4:5], v[4:5], v[198:199]
	v_med3_f32 v8, v8, s51, v155
	v_med3_f32 v9, v9, s51, v155
	v_med3_f32 v2, v4, s51, v155
	v_med3_f32 v3, v5, s51, v155
	v_cvt_pk_fp8_f32 v20, v8, v9 op_sel:[0,0,1]
	v_cvt_pk_fp8_f32 v21, v2, v3 op_sel:[0,0,1]
	global_store_dwordx2 v[18:19], v[20:21], off offset:1152
	s_cbranch_vccnz .LBB0_941
	s_andn2_b64 vcc, exec, s[6:7]
	s_cbranch_vccnz .LBB0_940
	s_barrier
	s_branch .LBB0_940
